# attention block selection: radix top-16 loop exits as soon as every token's threshold isolates exactly 16 keys (same selected set)
# speedup vs baseline: 1.0069x; 1.0030x over previous
; __device__ __forceinline__ void att_unit_mfma(KArgs args, int b, int qb, LAS unsigned char* lds, int wave0, int lane0, int tid0) {
;     ...
;           for (int k = 0; k < 8; ++k) { const int j = 8 * e8 + k; const float v = imp[(0 * 64 + stok) * 65 + j] * ilc[stok] + imp[(1 * 64 + stok) * 65 + j] * ilc[64 + stok] + imp[(2 * 64 + stok) * 65 + j] * ilc[128 + stok] + imp[(3 * 64 + stok) * 65 + j] * ilc[192 + stok];
;               const bool valid = j <= qb, forced = valid && (j == 0 || j == qb || j == qb - 1);
;               const unsigned bits_ = __builtin_bit_cast(unsigned, forced ? 1e30f : (valid ? v : -1e30f));
;               key[k] = ((bits_ ^ ((bits_ >> 31) ? 0xFFFFFFFFu : 0x80000000u)) & ~63u) | (unsigned)(63 - j); }
;           unsigned T = 0u;
; #pragma unroll 1
;     ...
; #pragma unroll
;               for (int k = 0; k < 8; ++k) c += key[k] >= cand ? 1 : 0;
;               c += __builtin_amdgcn_update_dpp(0, c, 0xB1, 0xf, 0xf, true);
;               c += __builtin_amdgcn_update_dpp(0, c, 0x4E, 0xf, 0xf, true);
;               c += __builtin_amdgcn_update_dpp(0, c, 0x141, 0xf, 0xf, true);
;               T = c >= NTOP ? cand : T; }
;           unsigned bits = 0u;
; #pragma unroll
;           for (int k = 0; k < 8; ++k) bits |= (key[k] >= T && 8 * e8 + k <= qb) ? (1u << k) : 0u;
;           if (bits) { __hip_atomic_fetch_or(maskw + stok * 2 + (e8 >> 2), bits << (8 * (e8 & 3)), __ATOMIC_RELAXED, __HIP_MEMORY_SCOPE_WORKGROUP); __hip_atomic_fetch_or(unionw + (e8 >> 2), bits << (8 * (e8 & 3)), __ATOMIC_RELAXED, __HIP_MEMORY_SCOPE_WORKGROUP); }
.LBB0_606:
	s_or_b64 exec, exec, s[6:7]
	v_cmp_lt_i32_e32 vcc, -1, v26
	s_movk_i32 s0, 0xffc0
	s_nop 0
	v_cndmask_b32_e32 v5, -1, v215, vcc
	v_cmp_lt_i32_e32 vcc, -1, v21
	v_bitop3_b32 v5, v5, s0, v26 bitop3:0x48
	v_sub_u32_e32 v5, v5, v23
	v_cndmask_b32_e32 v6, -1, v215, vcc
	v_cmp_lt_i32_e32 vcc, -1, v20
	v_bitop3_b32 v6, v6, s0, v21 bitop3:0x48
	v_sub_u32_e32 v6, v6, v22
	v_cndmask_b32_e32 v7, -1, v215, vcc
	v_cmp_lt_i32_e32 vcc, -1, v17
	v_bitop3_b32 v7, v7, s0, v20 bitop3:0x48
	v_sub_u32_e32 v7, v7, v19
	v_cndmask_b32_e32 v8, -1, v215, vcc
	v_cmp_lt_i32_e32 vcc, -1, v16
	v_bitop3_b32 v8, v8, s0, v17 bitop3:0x48
	v_sub_u32_e32 v8, v8, v18
	v_cndmask_b32_e32 v11, -1, v215, vcc
	v_cmp_lt_i32_e32 vcc, -1, v4
	v_bitop3_b32 v11, v11, s0, v16 bitop3:0x48
	v_sub_u32_e32 v11, v11, v13
	v_cndmask_b32_e32 v12, -1, v215, vcc
	v_bitop3_b32 v4, v12, s0, v4 bitop3:0x48
	v_sub_u32_e32 v4, v4, v10
	v_cmp_lt_i32_e32 vcc, -1, v9
	v_add_u32_e32 v10, 63, v4
	v_add_u32_e32 v5, 63, v5
	v_cndmask_b32_e32 v4, -1, v215, vcc
	v_bitop3_b32 v4, v4, s0, v9 bitop3:0x48
	v_sub_u32_e32 v4, v4, v3
	v_cmp_lt_i32_e32 vcc, -1, v24
	v_add_u32_e32 v12, 63, v4
	v_add_u32_e32 v6, 63, v6
	v_cndmask_b32_e32 v4, -1, v215, vcc
	v_bitop3_b32 v4, v4, s0, v24 bitop3:0x48
	v_sub_u32_e32 v4, v4, v25
	v_add_u32_e32 v7, 63, v7
	v_add_u32_e32 v8, 63, v8
	v_add_u32_e32 v11, 63, v11
	v_add_u32_e32 v4, 63, v4
	s_mov_b32 s0, 31
	v_mov_b32_e32 v9, 0
	s_mov_b64 s[100:101], 0
.LBB0_607:
	v_lshl_or_b32 v13, 1, s0, v9
	v_cmp_ge_u32_e32 vcc, v10, v13
	s_add_i32 s0, s0, -1
	s_cmp_eq_u32 s0, -1
	v_cndmask_b32_e64 v14, 0, 1, vcc
	v_cmp_ge_u32_e32 vcc, v12, v13
	s_nop 1
	v_addc_co_u32_e32 v14, vcc, 0, v14, vcc
	v_cmp_ge_u32_e32 vcc, v11, v13
	s_nop 1
	v_cndmask_b32_e64 v15, 0, 1, vcc
	v_cmp_ge_u32_e32 vcc, v8, v13
	s_nop 1
	v_addc_co_u32_e32 v14, vcc, v14, v15, vcc
	v_cmp_ge_u32_e32 vcc, v7, v13
	s_nop 1
	v_cndmask_b32_e64 v15, 0, 1, vcc
	v_cmp_ge_u32_e32 vcc, v6, v13
	s_nop 1
	v_addc_co_u32_e32 v14, vcc, v14, v15, vcc
	v_cmp_ge_u32_e32 vcc, v5, v13
	s_nop 1
	v_cndmask_b32_e64 v15, 0, 1, vcc
	v_cmp_ge_u32_e32 vcc, v4, v13
	s_nop 1
	v_addc_co_u32_e32 v14, vcc, v14, v15, vcc
	s_nop 1
	v_add_u32_dpp v14, v14, v14 quad_perm:[1,0,3,2] row_mask:0xf bank_mask:0xf bound_ctrl:1
	s_nop 1
	v_add_u32_dpp v14, v14, v14 quad_perm:[2,3,0,1] row_mask:0xf bank_mask:0xf bound_ctrl:1
	s_nop 1
	v_add_u32_dpp v14, v14, v14 row_half_mirror row_mask:0xf bank_mask:0xf bound_ctrl:1
	v_cmp_lt_i32_e32 vcc, 15, v14
	v_cmp_eq_u32_e64 s[4:5], 16, v14
	s_nop 0
	v_cndmask_b32_e32 v9, v9, v13, vcc
	s_or_b64 s[100:101], s[100:101], s[4:5]
	s_cmp_eq_u64 s[100:101], exec
	s_cbranch_scc1 .Lradix_done
	s_cmp_eq_u32 s0, -1
	s_cbranch_scc0 .LBB0_607
.Lradix_done:
	v_sub_u32_e32 v3, s2, v3
	v_cmp_ge_u32_e32 vcc, v12, v9
	v_cmp_lt_i32_e64 s[4:5], -1, v3
	s_and_b64 s[0:1], vcc, s[4:5]
	v_cmp_lt_u32_e32 vcc, v10, v9
	v_cmp_gt_i32_e64 s[4:5], 1, v3
	v_cndmask_b32_e64 v12, 0, 1, s[0:1]
	s_or_b64 s[0:1], vcc, s[4:5]
	v_cmp_lt_u32_e32 vcc, v11, v9
	v_cmp_gt_i32_e64 s[4:5], 2, v3
	v_cndmask_b32_e64 v10, 2, 0, s[0:1]
	s_or_b64 s[0:1], vcc, s[4:5]
	v_cmp_lt_u32_e32 vcc, v8, v9
	v_cmp_gt_i32_e64 s[4:5], 3, v3
	v_cndmask_b32_e64 v11, 4, 0, s[0:1]
	s_or_b64 s[0:1], vcc, s[4:5]
	v_cmp_lt_u32_e32 vcc, v7, v9
	v_cmp_gt_i32_e64 s[4:5], 4, v3
	v_cndmask_b32_e64 v8, 8, 0, s[0:1]
	s_or_b64 s[0:1], vcc, s[4:5]
	v_cmp_lt_u32_e32 vcc, v6, v9
	v_cmp_gt_i32_e64 s[4:5], 5, v3
	v_cndmask_b32_e64 v7, 16, 0, s[0:1]
	s_or_b64 s[0:1], vcc, s[4:5]
	v_cmp_lt_u32_e32 vcc, v5, v9
	v_cmp_gt_i32_e64 s[4:5], 6, v3
	v_or_b32_e32 v10, v10, v12
	v_cndmask_b32_e64 v6, 32, 0, s[0:1]
	s_or_b64 s[0:1], vcc, s[4:5]
	v_cmp_lt_u32_e32 vcc, v4, v9
	v_cmp_gt_i32_e64 s[4:5], 7, v3
	v_writelane_b32 v255, s48, 55
	v_or3_b32 v8, v10, v11, v8
	v_cndmask_b32_e64 v5, 64, 0, s[0:1]
	s_or_b64 s[0:1], vcc, s[4:5]
	v_writelane_b32 v255, s49, 56
	v_or3_b32 v6, v8, v7, v6
	v_cndmask_b32_e64 v3, v216, 0, s[0:1]
	v_writelane_b32 v255, s72, 57
	v_or3_b32 v3, v6, v5, v3
	s_mov_b32 s74, s47
	v_writelane_b32 v255, s73, 58
	v_cmp_ne_u32_e32 vcc, 0, v3
	s_and_saveexec_b64 s[4:5], vcc
	s_cbranch_execz .LBB0_610
	v_and_b32_e32 v4, -8, v1
	s_add_i32 s0, 0, 0x24500
	v_and_b32_e32 v2, 4, v2
	v_lshlrev_b32_e32 v1, 3, v1
	v_add3_u32 v4, s0, v4, v2
	v_lshlrev_b32_e32 v1, v1, v3
	v_add_u32_e32 v2, 0, v2
	v_add_u32_e32 v2, 0x24700, v2
	ds_or_b32 v4, v1
	ds_or_b32 v2, v1
